# grid barrier: workgroups other than an XCD's last arrival poll the top-level generation word directly (one relay hop less)
# speedup vs baseline: 1.0045x; 1.0045x over previous
; __device__ __forceinline__ unsigned xb_ld(unsigned* p)              { return __hip_atomic_load(p, __ATOMIC_RELAXED, __HIP_MEMORY_SCOPE_AGENT); }
; __device__ __forceinline__ unsigned xb_add(unsigned* p, unsigned v) { return __hip_atomic_fetch_add(p, v, __ATOMIC_RELAXED, __HIP_MEMORY_SCOPE_AGENT); }
; #define XB_SPIN(cond, bar) do { unsigned _sp = 0; while (cond) { __builtin_amdgcn_s_sleep(1); \
;     if ((++_sp & 255u) == 0u) { if (xb_ld(&(bar)[XB_TMO])) break; if (_sp > XB_SPIN_CAP) { atomicAdd(&(bar)[XB_TMO], 1u); break; } } } } while (0)
; __device__ __forceinline__ void xcd_barrier(const XcdBarrier& b) {
;     ...
;         const unsigned old = xb_add(&bar[XB_XSUB(b.x)], 1u);
;         const unsigned gen = old / nloc;
;         if (old + 1u == (gen + 1u) * nloc) {
;             __builtin_amdgcn_fence(__ATOMIC_RELEASE, "agent");
;             asm volatile("s_waitcnt vmcnt(0)" ::: "memory");
;             const unsigned og = xb_add(&bar[XB_TOP], 1u);
;             const unsigned tg = og / nx;
;             if (og + 1u == (tg + 1u) * nx) xb_add(&bar[XB_TOPGEN], 1u);
;             else XB_SPIN(xb_ld(&bar[XB_TOPGEN]) == tg, bar);
;             __builtin_amdgcn_fence(__ATOMIC_ACQUIRE, "agent");
;             xb_add(&bar[XB_XGEN(b.x)], 1u);
;             asm volatile("s_waitcnt vmcnt(0)" ::: "memory");
;         } else {
;             XB_SPIN(xb_ld(&bar[XB_XGEN(b.x)]) == gen, bar);
.LBB0_130:
	s_or_b64 exec, exec, s[18:19]
	v_cvt_f32_u32_e32 v6, v4
	s_waitcnt vmcnt(0)
	v_readfirstlane_b32 s0, v5
	s_add_u32 s8, s8, 0x2400
	s_addc_u32 s9, s9, 0
	v_rcp_iflag_f32_e32 v6, v6
	v_add_u32_e32 v7, s0, v3
	v_mul_f32_e32 v5, 0x4f7ffffe, v6
	v_cvt_u32_f32_e32 v5, v5
	v_sub_u32_e32 v6, 0, v4
	v_mul_lo_u32 v3, v6, v5
	v_mul_hi_u32 v3, v5, v3
	v_add_u32_e32 v3, v5, v3
	v_mul_hi_u32 v3, v7, v3
	v_mul_lo_u32 v5, v3, v4
	v_sub_u32_e32 v5, v7, v5
	v_add_u32_e32 v6, 1, v3
	v_cmp_ge_u32_e32 vcc, v5, v4
	s_nop 1
	v_cndmask_b32_e32 v3, v3, v6, vcc
	v_sub_u32_e32 v6, v5, v4
	v_cndmask_b32_e32 v5, v5, v6, vcc
	v_add_u32_e32 v6, 1, v3
	v_cmp_ge_u32_e32 vcc, v5, v4
	v_add_u32_e32 v5, 1, v7
	s_nop 0
	v_cndmask_b32_e32 v3, v3, v6, vcc
	v_mul_lo_u32 v6, v4, v3
	v_add_u32_e32 v4, v6, v4
	v_cmp_ne_u32_e32 vcc, v5, v4
	s_and_saveexec_b64 s[0:1], vcc
	s_xor_b64 s[12:13], exec, s[0:1]
	s_cbranch_execz .LBB0_144
	s_waitcnt lgkmcnt(0)
	s_lshl_b32 vcc_lo, s97, 8
	s_sub_u32 vcc_lo, 0x1100, vcc_lo
	v_mov_b32_e32 v2, vcc_lo
	global_load_dword v4, v2, s[8:9] sc1
	s_waitcnt vmcnt(0)
	v_cmp_eq_u32_e32 vcc, v4, v3
	s_and_saveexec_b64 s[18:19], vcc
	s_cbranch_execz .LBB0_143
	s_mov_b32 s0, 1
	s_mov_b64 s[20:21], 0
	s_branch .LBB0_134

; __device__ __forceinline__ unsigned xb_ld(unsigned* p)              { return __hip_atomic_load(p, __ATOMIC_RELAXED, __HIP_MEMORY_SCOPE_AGENT); }
; __device__ __forceinline__ unsigned xb_add(unsigned* p, unsigned v) { return __hip_atomic_fetch_add(p, v, __ATOMIC_RELAXED, __HIP_MEMORY_SCOPE_AGENT); }
; #define XB_SPIN(cond, bar) do { unsigned _sp = 0; while (cond) { __builtin_amdgcn_s_sleep(1); \
;     if ((++_sp & 255u) == 0u) { if (xb_ld(&(bar)[XB_TMO])) break; if (_sp > XB_SPIN_CAP) { atomicAdd(&(bar)[XB_TMO], 1u); break; } } } } while (0)
; __device__ __forceinline__ void xcd_barrier(const XcdBarrier& b) {
;     ...
;         const unsigned old = xb_add(&bar[XB_XSUB(b.x)], 1u);
;         const unsigned gen = old / nloc;
;         if (old + 1u == (gen + 1u) * nloc) {
;             __builtin_amdgcn_fence(__ATOMIC_RELEASE, "agent");
;             asm volatile("s_waitcnt vmcnt(0)" ::: "memory");
;             const unsigned og = xb_add(&bar[XB_TOP], 1u);
;             const unsigned tg = og / nx;
;             if (og + 1u == (tg + 1u) * nx) xb_add(&bar[XB_TOPGEN], 1u);
;             else XB_SPIN(xb_ld(&bar[XB_TOPGEN]) == tg, bar);
;             __builtin_amdgcn_fence(__ATOMIC_ACQUIRE, "agent");
;             xb_add(&bar[XB_XGEN(b.x)], 1u);
;             asm volatile("s_waitcnt vmcnt(0)" ::: "memory");
;         } else {
;             XB_SPIN(xb_ld(&bar[XB_XGEN(b.x)]) == gen, bar);
.LBB0_326:
	s_or_b64 exec, exec, s[14:15]
	v_cvt_f32_u32_e32 v6, v4
	s_waitcnt vmcnt(0)
	v_readfirstlane_b32 s0, v5
	s_add_u32 s8, s8, 0x2400
	s_addc_u32 s9, s9, 0
	v_rcp_iflag_f32_e32 v6, v6
	v_add_u32_e32 v7, s0, v3
	v_mul_f32_e32 v5, 0x4f7ffffe, v6
	v_cvt_u32_f32_e32 v5, v5
	v_sub_u32_e32 v6, 0, v4
	v_mul_lo_u32 v3, v6, v5
	v_mul_hi_u32 v3, v5, v3
	v_add_u32_e32 v3, v5, v3
	v_mul_hi_u32 v3, v7, v3
	v_mul_lo_u32 v5, v3, v4
	v_sub_u32_e32 v5, v7, v5
	v_add_u32_e32 v6, 1, v3
	v_cmp_ge_u32_e32 vcc, v5, v4
	s_nop 1
	v_cndmask_b32_e32 v3, v3, v6, vcc
	v_sub_u32_e32 v6, v5, v4
	v_cndmask_b32_e32 v5, v5, v6, vcc
	v_add_u32_e32 v6, 1, v3
	v_cmp_ge_u32_e32 vcc, v5, v4
	v_add_u32_e32 v5, 1, v7
	s_nop 0
	v_cndmask_b32_e32 v3, v3, v6, vcc
	v_mul_lo_u32 v6, v4, v3
	v_add_u32_e32 v4, v6, v4
	v_cmp_ne_u32_e32 vcc, v5, v4
	s_and_saveexec_b64 s[0:1], vcc
	s_xor_b64 s[12:13], exec, s[0:1]
	s_cbranch_execz .LBB0_340
	s_waitcnt lgkmcnt(0)
	s_lshl_b32 vcc_lo, s97, 8
	s_sub_u32 vcc_lo, 0x1100, vcc_lo
	v_mov_b32_e32 v2, vcc_lo
	global_load_dword v4, v2, s[8:9] sc1
	s_waitcnt vmcnt(0)
	v_cmp_eq_u32_e32 vcc, v4, v3
	s_and_saveexec_b64 s[14:15], vcc
	s_cbranch_execz .LBB0_339
	s_mov_b32 s0, 1
	s_mov_b64 s[20:21], 0
	s_branch .LBB0_330

; __device__ __forceinline__ unsigned xb_ld(unsigned* p)              { return __hip_atomic_load(p, __ATOMIC_RELAXED, __HIP_MEMORY_SCOPE_AGENT); }
; __device__ __forceinline__ unsigned xb_add(unsigned* p, unsigned v) { return __hip_atomic_fetch_add(p, v, __ATOMIC_RELAXED, __HIP_MEMORY_SCOPE_AGENT); }
; #define XB_SPIN(cond, bar) do { unsigned _sp = 0; while (cond) { __builtin_amdgcn_s_sleep(1); \
;     if ((++_sp & 255u) == 0u) { if (xb_ld(&(bar)[XB_TMO])) break; if (_sp > XB_SPIN_CAP) { atomicAdd(&(bar)[XB_TMO], 1u); break; } } } } while (0)
; __device__ __forceinline__ void xcd_barrier(const XcdBarrier& b) {
;     ...
;         const unsigned old = xb_add(&bar[XB_XSUB(b.x)], 1u);
;         const unsigned gen = old / nloc;
;         if (old + 1u == (gen + 1u) * nloc) {
;             __builtin_amdgcn_fence(__ATOMIC_RELEASE, "agent");
;             asm volatile("s_waitcnt vmcnt(0)" ::: "memory");
;             const unsigned og = xb_add(&bar[XB_TOP], 1u);
;             const unsigned tg = og / nx;
;             if (og + 1u == (tg + 1u) * nx) xb_add(&bar[XB_TOPGEN], 1u);
;             else XB_SPIN(xb_ld(&bar[XB_TOPGEN]) == tg, bar);
;             __builtin_amdgcn_fence(__ATOMIC_ACQUIRE, "agent");
;             xb_add(&bar[XB_XGEN(b.x)], 1u);
;             asm volatile("s_waitcnt vmcnt(0)" ::: "memory");
;         } else {
;             XB_SPIN(xb_ld(&bar[XB_XGEN(b.x)]) == gen, bar);
.LBB0_512:
	s_or_b64 exec, exec, s[22:23]
	v_cvt_f32_u32_e32 v6, v4
	s_waitcnt vmcnt(0)
	v_readfirstlane_b32 s0, v5
	s_add_u32 s12, s12, 0x2400
	s_addc_u32 s13, s13, 0
	v_rcp_iflag_f32_e32 v6, v6
	v_add_u32_e32 v7, s0, v3
	v_mul_f32_e32 v5, 0x4f7ffffe, v6
	v_cvt_u32_f32_e32 v5, v5
	v_sub_u32_e32 v6, 0, v4
	v_mul_lo_u32 v3, v6, v5
	v_mul_hi_u32 v3, v5, v3
	v_add_u32_e32 v3, v5, v3
	v_mul_hi_u32 v3, v7, v3
	v_mul_lo_u32 v5, v3, v4
	v_sub_u32_e32 v5, v7, v5
	v_add_u32_e32 v6, 1, v3
	v_cmp_ge_u32_e32 vcc, v5, v4
	s_nop 1
	v_cndmask_b32_e32 v3, v3, v6, vcc
	v_sub_u32_e32 v6, v5, v4
	v_cndmask_b32_e32 v5, v5, v6, vcc
	v_add_u32_e32 v6, 1, v3
	v_cmp_ge_u32_e32 vcc, v5, v4
	v_add_u32_e32 v5, 1, v7
	s_nop 0
	v_cndmask_b32_e32 v3, v3, v6, vcc
	v_mul_lo_u32 v6, v4, v3
	v_add_u32_e32 v4, v6, v4
	v_cmp_ne_u32_e32 vcc, v5, v4
	s_and_saveexec_b64 s[0:1], vcc
	s_xor_b64 s[14:15], exec, s[0:1]
	s_cbranch_execz .LBB0_526
	s_waitcnt lgkmcnt(0)
	s_lshl_b32 vcc_lo, s97, 8
	s_sub_u32 vcc_lo, 0x1100, vcc_lo
	v_mov_b32_e32 v2, vcc_lo
	global_load_dword v4, v2, s[12:13] sc1
	s_waitcnt vmcnt(0)
	v_cmp_eq_u32_e32 vcc, v4, v3
	s_and_saveexec_b64 s[22:23], vcc
	s_cbranch_execz .LBB0_525
	s_mov_b32 s0, 1
	s_mov_b64 s[24:25], 0
	s_branch .LBB0_516

; __device__ __forceinline__ unsigned xb_ld(unsigned* p)              { return __hip_atomic_load(p, __ATOMIC_RELAXED, __HIP_MEMORY_SCOPE_AGENT); }
; __device__ __forceinline__ unsigned xb_add(unsigned* p, unsigned v) { return __hip_atomic_fetch_add(p, v, __ATOMIC_RELAXED, __HIP_MEMORY_SCOPE_AGENT); }
; #define XB_SPIN(cond, bar) do { unsigned _sp = 0; while (cond) { __builtin_amdgcn_s_sleep(1); \
;     if ((++_sp & 255u) == 0u) { if (xb_ld(&(bar)[XB_TMO])) break; if (_sp > XB_SPIN_CAP) { atomicAdd(&(bar)[XB_TMO], 1u); break; } } } } while (0)
; __device__ __forceinline__ void xcd_barrier(const XcdBarrier& b) {
;     ...
;         const unsigned old = xb_add(&bar[XB_XSUB(b.x)], 1u);
;         const unsigned gen = old / nloc;
;         if (old + 1u == (gen + 1u) * nloc) {
;             __builtin_amdgcn_fence(__ATOMIC_RELEASE, "agent");
;             asm volatile("s_waitcnt vmcnt(0)" ::: "memory");
;             const unsigned og = xb_add(&bar[XB_TOP], 1u);
;             const unsigned tg = og / nx;
;             if (og + 1u == (tg + 1u) * nx) xb_add(&bar[XB_TOPGEN], 1u);
;             else XB_SPIN(xb_ld(&bar[XB_TOPGEN]) == tg, bar);
;             __builtin_amdgcn_fence(__ATOMIC_ACQUIRE, "agent");
;             xb_add(&bar[XB_XGEN(b.x)], 1u);
;             asm volatile("s_waitcnt vmcnt(0)" ::: "memory");
;         } else {
;             XB_SPIN(xb_ld(&bar[XB_XGEN(b.x)]) == gen, bar);
.LBB0_570:
	s_or_b64 exec, exec, s[20:21]
	v_cvt_f32_u32_e32 v6, v4
	s_waitcnt vmcnt(0)
	v_readfirstlane_b32 s0, v5
	s_add_u32 s8, s8, 0x2400
	s_addc_u32 s9, s9, 0
	v_rcp_iflag_f32_e32 v6, v6
	v_add_u32_e32 v7, s0, v3
	v_mul_f32_e32 v5, 0x4f7ffffe, v6
	v_cvt_u32_f32_e32 v5, v5
	v_sub_u32_e32 v6, 0, v4
	v_mul_lo_u32 v3, v6, v5
	v_mul_hi_u32 v3, v5, v3
	v_add_u32_e32 v3, v5, v3
	v_mul_hi_u32 v3, v7, v3
	v_mul_lo_u32 v5, v3, v4
	v_sub_u32_e32 v5, v7, v5
	v_add_u32_e32 v6, 1, v3
	v_cmp_ge_u32_e32 vcc, v5, v4
	s_nop 1
	v_cndmask_b32_e32 v3, v3, v6, vcc
	v_sub_u32_e32 v6, v5, v4
	v_cndmask_b32_e32 v5, v5, v6, vcc
	v_add_u32_e32 v6, 1, v3
	v_cmp_ge_u32_e32 vcc, v5, v4
	v_add_u32_e32 v5, 1, v7
	s_nop 0
	v_cndmask_b32_e32 v3, v3, v6, vcc
	v_mul_lo_u32 v6, v4, v3
	v_add_u32_e32 v4, v6, v4
	v_cmp_ne_u32_e32 vcc, v5, v4
	s_and_saveexec_b64 s[0:1], vcc
	s_xor_b64 s[14:15], exec, s[0:1]
	s_cbranch_execz .LBB0_584
	s_waitcnt lgkmcnt(0)
	s_lshl_b32 vcc_lo, s97, 8
	s_sub_u32 vcc_lo, 0x1100, vcc_lo
	v_mov_b32_e32 v2, vcc_lo
	global_load_dword v4, v2, s[8:9] sc1
	s_waitcnt vmcnt(0)
	v_cmp_eq_u32_e32 vcc, v4, v3
	s_and_saveexec_b64 s[20:21], vcc
	s_cbranch_execz .LBB0_583
	s_mov_b32 s0, 1
	s_mov_b64 s[22:23], 0
	s_branch .LBB0_574

; __device__ __forceinline__ unsigned xb_ld(unsigned* p)              { return __hip_atomic_load(p, __ATOMIC_RELAXED, __HIP_MEMORY_SCOPE_AGENT); }
; __device__ __forceinline__ unsigned xb_add(unsigned* p, unsigned v) { return __hip_atomic_fetch_add(p, v, __ATOMIC_RELAXED, __HIP_MEMORY_SCOPE_AGENT); }
; #define XB_SPIN(cond, bar) do { unsigned _sp = 0; while (cond) { __builtin_amdgcn_s_sleep(1); \
;     if ((++_sp & 255u) == 0u) { if (xb_ld(&(bar)[XB_TMO])) break; if (_sp > XB_SPIN_CAP) { atomicAdd(&(bar)[XB_TMO], 1u); break; } } } } while (0)
; __device__ __forceinline__ void xcd_barrier(const XcdBarrier& b) {
;     ...
;         const unsigned old = xb_add(&bar[XB_XSUB(b.x)], 1u);
;         const unsigned gen = old / nloc;
;         if (old + 1u == (gen + 1u) * nloc) {
;             __builtin_amdgcn_fence(__ATOMIC_RELEASE, "agent");
;             asm volatile("s_waitcnt vmcnt(0)" ::: "memory");
;             const unsigned og = xb_add(&bar[XB_TOP], 1u);
;             const unsigned tg = og / nx;
;             if (og + 1u == (tg + 1u) * nx) xb_add(&bar[XB_TOPGEN], 1u);
;             else XB_SPIN(xb_ld(&bar[XB_TOPGEN]) == tg, bar);
;             __builtin_amdgcn_fence(__ATOMIC_ACQUIRE, "agent");
;             xb_add(&bar[XB_XGEN(b.x)], 1u);
;             asm volatile("s_waitcnt vmcnt(0)" ::: "memory");
;         } else {
;             XB_SPIN(xb_ld(&bar[XB_XGEN(b.x)]) == gen, bar);
.LBB0_774:
	s_or_b64 exec, exec, s[14:15]
	v_cvt_f32_u32_e32 v6, v4
	s_waitcnt vmcnt(0)
	v_readfirstlane_b32 s10, v5
	s_add_u32 s6, s6, 0x2400
	s_addc_u32 s7, s7, 0
	v_rcp_iflag_f32_e32 v6, v6
	v_add_u32_e32 v7, s10, v3
	v_mul_f32_e32 v5, 0x4f7ffffe, v6
	v_cvt_u32_f32_e32 v5, v5
	v_sub_u32_e32 v6, 0, v4
	v_mul_lo_u32 v3, v6, v5
	v_mul_hi_u32 v3, v5, v3
	v_add_u32_e32 v3, v5, v3
	v_mul_hi_u32 v3, v7, v3
	v_mul_lo_u32 v5, v3, v4
	v_sub_u32_e32 v5, v7, v5
	v_add_u32_e32 v6, 1, v3
	v_cmp_ge_u32_e32 vcc, v5, v4
	s_nop 1
	v_cndmask_b32_e32 v3, v3, v6, vcc
	v_sub_u32_e32 v6, v5, v4
	v_cndmask_b32_e32 v5, v5, v6, vcc
	v_add_u32_e32 v6, 1, v3
	v_cmp_ge_u32_e32 vcc, v5, v4
	v_add_u32_e32 v5, 1, v7
	s_nop 0
	v_cndmask_b32_e32 v3, v3, v6, vcc
	v_mul_lo_u32 v6, v4, v3
	v_add_u32_e32 v4, v6, v4
	v_cmp_ne_u32_e32 vcc, v5, v4
	s_and_saveexec_b64 s[10:11], vcc
	s_xor_b64 s[12:13], exec, s[10:11]
	s_cbranch_execz .LBB0_788
	s_waitcnt lgkmcnt(0)
	s_lshl_b32 vcc_lo, s97, 8
	s_sub_u32 vcc_lo, 0x1100, vcc_lo
	v_mov_b32_e32 v2, vcc_lo
	global_load_dword v4, v2, s[6:7] sc1
	s_waitcnt vmcnt(0)
	v_cmp_eq_u32_e32 vcc, v4, v3
	s_and_saveexec_b64 s[14:15], vcc
	s_cbranch_execz .LBB0_787
	s_mov_b32 s10, 1
	s_mov_b64 s[16:17], 0
	s_branch .LBB0_778

; __device__ __forceinline__ unsigned xb_ld(unsigned* p)              { return __hip_atomic_load(p, __ATOMIC_RELAXED, __HIP_MEMORY_SCOPE_AGENT); }
; __device__ __forceinline__ unsigned xb_add(unsigned* p, unsigned v) { return __hip_atomic_fetch_add(p, v, __ATOMIC_RELAXED, __HIP_MEMORY_SCOPE_AGENT); }
; #define XB_SPIN(cond, bar) do { unsigned _sp = 0; while (cond) { __builtin_amdgcn_s_sleep(1); \
;     if ((++_sp & 255u) == 0u) { if (xb_ld(&(bar)[XB_TMO])) break; if (_sp > XB_SPIN_CAP) { atomicAdd(&(bar)[XB_TMO], 1u); break; } } } } while (0)
; __device__ __forceinline__ void xcd_barrier(const XcdBarrier& b) {
;     ...
;         const unsigned old = xb_add(&bar[XB_XSUB(b.x)], 1u);
;         const unsigned gen = old / nloc;
;         if (old + 1u == (gen + 1u) * nloc) {
;             __builtin_amdgcn_fence(__ATOMIC_RELEASE, "agent");
;             asm volatile("s_waitcnt vmcnt(0)" ::: "memory");
;             const unsigned og = xb_add(&bar[XB_TOP], 1u);
;             const unsigned tg = og / nx;
;             if (og + 1u == (tg + 1u) * nx) xb_add(&bar[XB_TOPGEN], 1u);
;             else XB_SPIN(xb_ld(&bar[XB_TOPGEN]) == tg, bar);
;             __builtin_amdgcn_fence(__ATOMIC_ACQUIRE, "agent");
;             xb_add(&bar[XB_XGEN(b.x)], 1u);
;             asm volatile("s_waitcnt vmcnt(0)" ::: "memory");
;         } else {
;             XB_SPIN(xb_ld(&bar[XB_XGEN(b.x)]) == gen, bar);
.LBB0_854:
	s_or_b64 exec, exec, s[10:11]
	v_cvt_f32_u32_e32 v6, v4
	s_waitcnt vmcnt(0)
	v_readfirstlane_b32 s8, v5
	s_add_u32 s6, s6, 0x2400
	s_addc_u32 s7, s7, 0
	v_rcp_iflag_f32_e32 v6, v6
	v_add_u32_e32 v7, s8, v3
	v_mul_f32_e32 v5, 0x4f7ffffe, v6
	v_cvt_u32_f32_e32 v5, v5
	v_sub_u32_e32 v6, 0, v4
	v_mul_lo_u32 v3, v6, v5
	v_mul_hi_u32 v3, v5, v3
	v_add_u32_e32 v3, v5, v3
	v_mul_hi_u32 v3, v7, v3
	v_mul_lo_u32 v5, v3, v4
	v_sub_u32_e32 v5, v7, v5
	v_add_u32_e32 v6, 1, v3
	v_cmp_ge_u32_e32 vcc, v5, v4
	s_nop 1
	v_cndmask_b32_e32 v3, v3, v6, vcc
	v_sub_u32_e32 v6, v5, v4
	v_cndmask_b32_e32 v5, v5, v6, vcc
	v_add_u32_e32 v6, 1, v3
	v_cmp_ge_u32_e32 vcc, v5, v4
	v_add_u32_e32 v5, 1, v7
	s_nop 0
	v_cndmask_b32_e32 v3, v3, v6, vcc
	v_mul_lo_u32 v6, v4, v3
	v_add_u32_e32 v4, v6, v4
	v_cmp_ne_u32_e32 vcc, v5, v4
	s_and_saveexec_b64 s[8:9], vcc
	s_xor_b64 s[8:9], exec, s[8:9]
	s_cbranch_execz .LBB0_868
	s_waitcnt lgkmcnt(0)
	s_lshl_b32 vcc_lo, s97, 8
	s_sub_u32 vcc_lo, 0x1100, vcc_lo
	v_mov_b32_e32 v2, vcc_lo
	global_load_dword v4, v2, s[6:7] sc1
	s_waitcnt vmcnt(0)
	v_cmp_eq_u32_e32 vcc, v4, v3
	s_and_saveexec_b64 s[10:11], vcc
	s_cbranch_execz .LBB0_867
	s_mov_b32 s22, 1
	s_mov_b64 s[12:13], 0
	s_branch .LBB0_858
